# P2c ml_out: second half of chunk-start C^T staged once per workgroup through free LDS by DMA (was 16 late 4x-redundant global loads per wave); early touch of the normaliser-state lines
# baseline (speedup 1.0000x reference)
; #define LAS __attribute__((address_space(3)))
; __device__ __forceinline__ void ml_out_phase(const Params& p, Frame& F) {
;     ...
;         { const bf16_t* CT = (const bf16_t*)(ws + WS_CST) + (size_t)item * 32768;
; #pragma unroll
;           for (int nb = 0; nb < 4; ++nb)
; #pragma unroll
;               for (int ks = 0; ks < 4; ++ks) ctf[nb][ks] = *(const bf16x8*)(CT + (size_t)(16 * (8 * vh + nb) + fr) * 128 + 32 * ks + 8 * fq); }
;         __builtin_amdgcn_sched_barrier(0);
;         if (w == 0) {
;             float g = lf;
; #pragma unroll
;             for (int o = 1; o < 64; o <<= 1) { const float v = __shfl_up(g, o); if (lane >= o) g += v; }
;             const float a = li - g; float pm = a;
; #pragma unroll
;             for (int o = 1; o < 64; o <<= 1) { const float v = __shfl_up(pm, o); if (lane >= o) pm = fmaxf(pm, v); }
;             const float M = fmaxf(mst, pm);
;             int ln = lane; asm volatile("" : "+v"(ln)); LAS float* gs = avec + ln;
;             gs[0] = a; gs[64] = M; gs[128] = __expf(mst - M); gs[192] = __expf(-(g + M));
;         }
;     ...
;         { const bf16_t* CT = (const bf16_t*)(ws + WS_CST) + (size_t)item * 32768;
; #pragma unroll
;           for (int nb = 0; nb < 4; ++nb)
; #pragma unroll
;               for (int ks = 0; ks < 4; ++ks) ctg[nb][ks] = *(const bf16x8*)(CT + (size_t)(16 * (8 * vh + 4 + nb) + fr) * 128 + 32 * ks + 8 * fq); }
.LBB0_611:
	s_or_b64 exec, exec, s[0:1]
	s_ashr_i32 s91, s90, 31
	s_lshl_b64 s[0:1], s[90:91], 16
	v_lshl_add_u64 v[152:153], v[132:133], 0, s[0:1]
	v_readlane_b32 s98, v245, 63
	s_nop 3
	s_lshr_b32 s98, s98, 1
	s_and_b32 s100, s98, 3
	s_lshl_b32 s100, s100, 12
	s_mov_b32 s101, 0
	v_lshl_add_u64 v[246:247], v[152:153], 0, v[142:143]
	s_nop 1
	v_lshl_add_u64 v[246:247], v[246:247], 0, s[100:101]
	s_lshl_b32 s99, s98, 12
	s_add_i32 s99, s99, 0x1f000
	s_mov_b64 s[100:101], 64
	s_mov_b32 m0, s99
	s_addk_i32 s99, 0x400
	global_load_lds_dwordx4 v[246:247], off
	v_lshl_add_u64 v[246:247], v[246:247], 0, s[100:101]
	s_mov_b32 m0, s99
	s_addk_i32 s99, 0x400
	global_load_lds_dwordx4 v[246:247], off
	v_lshl_add_u64 v[246:247], v[246:247], 0, s[100:101]
	s_mov_b32 m0, s99
	s_addk_i32 s99, 0x400
	global_load_lds_dwordx4 v[246:247], off
	v_lshl_add_u64 v[246:247], v[246:247], 0, s[100:101]
	s_mov_b32 m0, s99
	s_addk_i32 s99, 0x400
	global_load_lds_dwordx4 v[246:247], off
	s_nop 0
	v_mbcnt_lo_u32_b32 v246, -1, 0
	v_mbcnt_hi_u32_b32 v246, -1, v246
	s_lshr_b32 s99, s98, 2
	s_lshl_b32 s99, s99, 14
	s_add_i32 s99, s99, 0x1f000
	v_lshl_add_u32 v246, v246, 4, s99
	s_lshl_b64 s[100:101], s[90:91], 9
	s_add_u32 s100, s100, s96
	s_addc_u32 s101, s101, s97
	s_add_u32 s100, s100, 0x880000
	s_addc_u32 s101, s101, 0
	v_mbcnt_lo_u32_b32 v247, -1, 0
	v_mbcnt_hi_u32_b32 v247, -1, v247
	v_lshlrev_b32_e32 v247, 3, v247
	global_load_dword v247, v247, s[100:101]
	v_lshl_add_u64 v[2:3], v[152:153], 0, v[134:135]
	global_load_dwordx4 v[62:65], v[2:3], off
	global_load_dwordx4 v[58:61], v[2:3], off offset:64
	global_load_dwordx4 v[54:57], v[2:3], off offset:128
	global_load_dwordx4 v[50:53], v[2:3], off offset:192
	v_lshl_add_u64 v[2:3], v[152:153], 0, v[136:137]
	global_load_dwordx4 v[46:49], v[2:3], off
	global_load_dwordx4 v[42:45], v[2:3], off offset:64
	global_load_dwordx4 v[38:41], v[2:3], off offset:128
	global_load_dwordx4 v[34:37], v[2:3], off offset:192
	v_lshl_add_u64 v[2:3], v[152:153], 0, v[138:139]
	global_load_dwordx4 v[30:33], v[2:3], off
	global_load_dwordx4 v[26:29], v[2:3], off offset:64
	global_load_dwordx4 v[22:25], v[2:3], off offset:128
	global_load_dwordx4 v[18:21], v[2:3], off offset:192
	v_lshl_add_u64 v[2:3], v[152:153], 0, v[140:141]
	global_load_dwordx4 v[14:17], v[2:3], off
	global_load_dwordx4 v[10:13], v[2:3], off offset:64
	global_load_dwordx4 v[6:9], v[2:3], off offset:128
	s_nop 0
	global_load_dwordx4 v[2:5], v[2:3], off offset:192
	s_andn2_b64 vcc, exec, s[16:17]
	v_mbcnt_hi_u32_b32 v128, -1, v223
	s_cbranch_vccnz .LBB0_613
	v_and_b32_e32 v66, 64, v128
	v_add_u32_e32 v67, -1, v128
	v_cmp_lt_i32_e32 vcc, v67, v66
	v_add_u32_e32 v69, -2, v128
	v_readlane_b32 s0, v244, 16
	v_cndmask_b32_e32 v67, v67, v128, vcc
	v_lshlrev_b32_e32 v67, 2, v67
	ds_bpermute_b32 v68, v67, v155
	v_cmp_lt_i32_e32 vcc, v69, v66
	v_readlane_b32 s1, v244, 17
	v_readlane_b32 s4, v244, 18
	v_cndmask_b32_e32 v69, v69, v128, vcc
	s_waitcnt lgkmcnt(0)
	v_add_f32_e32 v68, v155, v68
	v_cndmask_b32_e64 v68, v68, v155, s[0:1]
	v_lshlrev_b32_e32 v69, 2, v69
	ds_bpermute_b32 v70, v69, v68
	v_readlane_b32 s5, v244, 19
	v_readlane_b32 s20, v244, 20
	v_readlane_b32 s21, v244, 21
	s_mov_b32 s13, s23
	s_waitcnt lgkmcnt(0)
	v_add_f32_e32 v70, v68, v70
	v_cndmask_b32_e64 v68, v70, v68, s[4:5]
	v_add_u32_e32 v70, -4, v128
	v_cmp_lt_i32_e32 vcc, v70, v66
	v_readlane_b32 s22, v244, 22
	v_readlane_b32 s23, v244, 23
	v_cndmask_b32_e32 v70, v70, v128, vcc
	v_lshlrev_b32_e32 v70, 2, v70
	ds_bpermute_b32 v71, v70, v68
	v_readlane_b32 s24, v245, 59
	v_readlane_b32 s25, v245, 60
	s_waitcnt lgkmcnt(0)
	v_add_f32_e32 v71, v68, v71
	v_cndmask_b32_e64 v68, v71, v68, s[20:21]
	v_add_u32_e32 v71, -8, v128
	v_cmp_lt_i32_e32 vcc, v71, v66
	s_nop 1
	v_cndmask_b32_e32 v71, v71, v128, vcc
	v_lshlrev_b32_e32 v71, 2, v71
	ds_bpermute_b32 v72, v71, v68
	s_waitcnt lgkmcnt(0)
	v_add_f32_e32 v72, v68, v72
	v_cndmask_b32_e64 v68, v72, v68, s[22:23]
	v_add_u32_e32 v72, -16, v128
	v_cmp_lt_i32_e32 vcc, v72, v66
	s_nop 1
	v_cndmask_b32_e32 v72, v72, v128, vcc
	v_lshlrev_b32_e32 v72, 2, v72
	ds_bpermute_b32 v73, v72, v68
	s_waitcnt lgkmcnt(0)
	v_add_f32_e32 v73, v68, v73
	v_cndmask_b32_e64 v68, v73, v68, s[2:3]
	v_subrev_u32_e32 v73, 32, v128
	v_cmp_lt_i32_e32 vcc, v73, v66
	s_nop 1
	v_cndmask_b32_e32 v66, v73, v128, vcc
	v_lshlrev_b32_e32 v66, 2, v66
	ds_bpermute_b32 v73, v66, v68
	s_waitcnt lgkmcnt(0)
	v_add_f32_e32 v73, v68, v73
	v_cndmask_b32_e64 v68, v73, v68, s[24:25]
	v_sub_f32_e32 v73, v154, v68
	ds_bpermute_b32 v67, v67, v73
	s_waitcnt lgkmcnt(0)
	v_max_f32_e32 v67, v67, v67
	v_max_f32_e32 v67, v73, v67
	v_cndmask_b32_e64 v67, v67, v73, s[0:1]
	ds_bpermute_b32 v69, v69, v67
	s_waitcnt lgkmcnt(0)
	v_max_f32_e32 v69, v69, v69
	v_max_f32_e32 v69, v67, v69
	v_cndmask_b32_e64 v67, v69, v67, s[4:5]
	ds_bpermute_b32 v69, v70, v67
	s_waitcnt lgkmcnt(0)
	v_max_f32_e32 v69, v69, v69
	v_max_f32_e32 v69, v67, v69
	v_cndmask_b32_e64 v67, v69, v67, s[20:21]
	ds_bpermute_b32 v69, v71, v67
	s_waitcnt lgkmcnt(0)
	v_max_f32_e32 v69, v69, v69
	v_max_f32_e32 v69, v67, v69
	v_cndmask_b32_e64 v67, v69, v67, s[22:23]
	ds_bpermute_b32 v69, v72, v67
	s_mov_b32 s23, s13
	s_waitcnt lgkmcnt(0)
	v_max_f32_e32 v69, v69, v69
	v_max_f32_e32 v69, v67, v69
	v_cndmask_b32_e64 v67, v69, v67, s[2:3]
	ds_bpermute_b32 v66, v66, v67
	v_max_f32_e32 v69, v67, v67
	s_waitcnt lgkmcnt(0)
	v_max_f32_e32 v66, v66, v66
	v_max_f32_e32 v66, v69, v66
	v_cndmask_b32_e64 v66, v66, v67, s[24:25]
	v_max_f32_e32 v66, v66, v66
	v_max_f32_e32 v67, v156, v156
	v_max_f32_e32 v66, v67, v66
	v_mov_b32_e32 v67, v162
	v_sub_f32_e32 v69, v156, v66
	v_lshl_add_u32 v67, v67, 2, 0
	v_add_u32_e32 v67, 0x1e000, v67
	ds_write2st64_b32 v67, v73, v66 offset1:1
	v_add_f32_e32 v66, v68, v66
	v_mul_f32_e32 v69, 0x3fb8aa3b, v69
	v_mul_f32_e32 v66, 0xbfb8aa3b, v66
	v_exp_f32_e32 v69, v69
	v_exp_f32_e32 v66, v66
	ds_write2st64_b32 v67, v69, v66 offset0:2 offset1:3

; __device__ __forceinline__ float sigmoidf_(float x) { return __builtin_amdgcn_rcpf(1.0f + __expf(-x)); }
; __device__ __forceinline__ bf16_t f2bf(float v) { return (bf16_t)(cvt_pk_bf16(v, 0.f) & 0xffffu); }
; __device__ __forceinline__ void ml_out_phase(const Params& p, Frame& F) {
;     ...
;         { const float q0 = cwv[0], q1 = cwv[1], q2 = cwv[2], q3 = cwv[3], qb = cwv[4], k0 = cwv[5], k1 = cwv[6], k2 = cwv[7], k3 = cwv[8], kb = cwv[9];
; #pragma unroll
;           for (int j = 0; j < 16; ++j) { const float a = qb + q0 * rq[j] + q1 * rq[j + 1] + q2 * rq[j + 2] + q3 * rq[j + 3]; const float bq = kb + k0 * rk[j] + k1 * rk[j + 1] + k2 * rk[j + 2] + k3 * rk[j + 3];
;               const int t = 16 * tq + j, sw = t * 128 + ((((d >> 3) ^ (t & 15)) << 3) | (d & 7));
;               QR[sw] = f2bf(a * sigmoidf_(a) * 0.08838834764831845f); KR[sw] = f2bf(bq * sigmoidf_(bq)); } }
.LBB0_616:
	s_and_b32 s0, s90, 0x7f
	s_cmp_eq_u32 s0, 0
	s_cselect_b64 s[0:1], -1, 0
	s_and_b64 s[4:5], s[0:1], s[26:27]
	s_waitcnt lgkmcnt(0)
	v_lshlrev_b32_e32 v66, 16, v85
	v_cndmask_b32_e64 v109, v66, 0, s[4:5]
	s_and_b64 s[0:1], s[0:1], s[28:29]
	v_lshlrev_b32_e32 v66, 16, v81
	v_cndmask_b32_e64 v111, v66, 0, s[0:1]
	v_lshlrev_b32_e32 v66, 16, v73
	v_lshlrev_b32_e32 v92, 16, v80
	v_lshlrev_b32_e32 v80, 16, v78
	v_lshlrev_b32_e32 v78, 16, v94
	v_fma_f32 v94, v174, v109, v175
	v_cndmask_b32_e64 v113, v66, 0, s[4:5]
	v_fmac_f32_e32 v94, v167, v111
	v_lshlrev_b32_e32 v115, 16, v68
	v_fmac_f32_e32 v94, v168, v113
	v_fmac_f32_e32 v94, v171, v115
	v_lshlrev_b32_e32 v118, 16, v86
	v_lshlrev_b32_e32 v86, 16, v75
	v_lshlrev_b32_e32 v75, 16, v96
	v_mul_f32_e32 v96, 0xbfb8aa3b, v94
	v_exp_f32_e32 v96, v96
	v_lshlrev_b32_e32 v67, 16, v90
	v_cndmask_b32_e64 v110, v67, 0, s[4:5]
	v_lshlrev_b32_e32 v67, 16, v89
	v_add_f32_e32 v96, 1.0, v96
	v_rcp_f32_e32 v96, v96
	v_cndmask_b32_e64 v112, v67, 0, s[0:1]
	v_lshlrev_b32_e32 v67, 16, v88
	v_lshlrev_b32_e32 v85, 16, v83
	v_lshlrev_b32_e32 v83, 16, v82
	v_lshlrev_b32_e32 v82, 16, v77
	v_lshlrev_b32_e32 v77, 16, v95
	v_fma_f32 v95, v173, v110, v172
	v_cndmask_b32_e64 v114, v67, 0, s[4:5]
	v_fmac_f32_e32 v95, v169, v112
	v_mul_f32_e32 v94, v94, v96
	v_lshlrev_b32_e32 v116, 16, v87
	v_fmac_f32_e32 v95, v166, v114
	v_mul_f32_e32 v94, 0x3db504f3, v94
	v_fmac_f32_e32 v95, v170, v116
	v_cvt_pk_bf16_f32 v94, v94, s0
	ds_write_b16 v176, v94
	v_mul_f32_e32 v94, 0xbfb8aa3b, v95
	v_exp_f32_e32 v94, v94
	v_lshlrev_b32_e32 v117, 16, v69
	v_lshlrev_b32_e32 v93, 16, v70
	v_lshlrev_b32_e32 v91, 16, v71
	v_add_f32_e32 v94, 1.0, v94
	v_rcp_f32_e32 v94, v94
	v_lshlrev_b32_e32 v90, 16, v79
	v_lshlrev_b32_e32 v89, 16, v72
	v_lshlrev_b32_e32 v88, 16, v74
	v_mul_f32_e32 v94, v95, v94
	v_cvt_pk_bf16_f32 v94, v94, s0
	ds_write_b16 v176, v94 offset:17408
	v_fma_f32 v94, v174, v111, v175
	v_fmac_f32_e32 v94, v167, v113
	v_fmac_f32_e32 v94, v168, v115
	v_fmac_f32_e32 v94, v171, v117
	v_mul_f32_e32 v96, 0xbfb8aa3b, v94
	v_exp_f32_e32 v96, v96
	v_fma_f32 v95, v173, v112, v172
	v_fmac_f32_e32 v95, v169, v114
	v_fmac_f32_e32 v95, v166, v116
	v_add_f32_e32 v96, 1.0, v96
	v_rcp_f32_e32 v96, v96
	v_fmac_f32_e32 v95, v170, v118
	v_lshlrev_b32_e32 v87, 16, v84
	v_lshlrev_b32_e32 v84, 16, v76
	v_mul_f32_e32 v94, v94, v96
	v_mul_f32_e32 v94, 0x3db504f3, v94
	v_cvt_pk_bf16_f32 v94, v94, s0
	ds_write_b16 v177, v94 offset:256
	v_mul_f32_e32 v94, 0xbfb8aa3b, v95
	v_exp_f32_e32 v94, v94
	v_lshlrev_b32_e32 v81, 16, v99
	v_lshlrev_b32_e32 v79, 16, v98
	v_lshlrev_b32_e32 v76, 16, v108
	v_add_f32_e32 v94, 1.0, v94
	v_rcp_f32_e32 v94, v94
	v_lshlrev_b32_e32 v74, 16, v107
	v_lshlrev_b32_e32 v70, 16, v97
	v_lshlrev_b32_e32 v66, 16, v106
	v_mul_f32_e32 v94, v95, v94
	v_cvt_pk_bf16_f32 v94, v94, s0
	ds_write_b16 v177, v94 offset:17664
	v_fma_f32 v94, v174, v113, v175
	v_fmac_f32_e32 v94, v167, v115
	v_fmac_f32_e32 v94, v168, v117
	v_fmac_f32_e32 v94, v171, v93
	v_mul_f32_e32 v96, 0xbfb8aa3b, v94
	v_exp_f32_e32 v96, v96
	v_fma_f32 v95, v173, v114, v172
	v_fmac_f32_e32 v95, v169, v116
	v_fmac_f32_e32 v95, v166, v118
	v_add_f32_e32 v96, 1.0, v96
	v_rcp_f32_e32 v96, v96
	v_fmac_f32_e32 v95, v170, v92
	v_lshlrev_b32_e32 v71, 16, v100
	v_lshlrev_b32_e32 v67, 16, v105
	v_mul_f32_e32 v94, v94, v96
	v_mul_f32_e32 v94, 0x3db504f3, v94
	v_cvt_pk_bf16_f32 v94, v94, s0
	ds_write_b16 v178, v94 offset:512
	v_mul_f32_e32 v94, 0xbfb8aa3b, v95
	v_exp_f32_e32 v94, v94
	v_lshlrev_b32_e32 v72, 16, v101
	v_lshlrev_b32_e32 v73, 16, v102
	v_lshlrev_b32_e32 v68, 16, v104
	v_add_f32_e32 v94, 1.0, v94
	v_rcp_f32_e32 v94, v94
	v_lshlrev_b32_e32 v69, 16, v103
	v_mul_f32_e32 v94, v95, v94
	v_cvt_pk_bf16_f32 v94, v94, s0
	ds_write_b16 v178, v94 offset:17920
	v_fma_f32 v94, v174, v115, v175
	v_fmac_f32_e32 v94, v167, v117
	v_fmac_f32_e32 v94, v168, v93
	v_fmac_f32_e32 v94, v171, v91
	v_mul_f32_e32 v96, 0xbfb8aa3b, v94
	v_exp_f32_e32 v96, v96
	v_fma_f32 v95, v173, v116, v172
	v_fmac_f32_e32 v95, v169, v118
	v_fmac_f32_e32 v95, v166, v92
	v_add_f32_e32 v96, 1.0, v96
	v_rcp_f32_e32 v96, v96
	v_fmac_f32_e32 v95, v170, v90
	v_mul_f32_e32 v94, v94, v96
	v_mul_f32_e32 v94, 0x3db504f3, v94
	v_cvt_pk_bf16_f32 v94, v94, s0
	ds_write_b16 v179, v94 offset:768
	v_mul_f32_e32 v94, 0xbfb8aa3b, v95
	v_exp_f32_e32 v94, v94
	s_nop 0
	v_add_f32_e32 v94, 1.0, v94
	v_rcp_f32_e32 v94, v94
	s_nop 0
	v_mul_f32_e32 v94, v95, v94
	v_cvt_pk_bf16_f32 v94, v94, s0
	ds_write_b16 v179, v94 offset:18176
	v_fma_f32 v94, v174, v117, v175
	v_fmac_f32_e32 v94, v167, v93
	v_fmac_f32_e32 v94, v168, v91
	v_fmac_f32_e32 v94, v171, v89
	v_mul_f32_e32 v96, 0xbfb8aa3b, v94
	v_exp_f32_e32 v96, v96
	v_fma_f32 v95, v173, v118, v172
	v_fmac_f32_e32 v95, v169, v92
	v_fmac_f32_e32 v95, v166, v90
	v_add_f32_e32 v96, 1.0, v96
	v_rcp_f32_e32 v96, v96
	v_fmac_f32_e32 v95, v170, v88
	v_fma_f32 v93, v174, v93, v175
	v_fmac_f32_e32 v93, v167, v91
	v_mul_f32_e32 v94, v94, v96
	v_mul_f32_e32 v94, 0x3db504f3, v94
	v_cvt_pk_bf16_f32 v94, v94, s0
	ds_write_b16 v180, v94 offset:1024
	v_mul_f32_e32 v94, 0xbfb8aa3b, v95
	v_exp_f32_e32 v94, v94
	v_fmac_f32_e32 v93, v168, v89
	v_fmac_f32_e32 v93, v171, v87
	v_fma_f32 v92, v173, v92, v172
	v_add_f32_e32 v94, 1.0, v94
	v_rcp_f32_e32 v94, v94
	v_fmac_f32_e32 v92, v169, v90
	v_fmac_f32_e32 v92, v166, v88
	v_fmac_f32_e32 v92, v170, v86
	v_mul_f32_e32 v94, v95, v94
	v_cvt_pk_bf16_f32 v94, v94, s0
	ds_write_b16 v180, v94 offset:18432
	v_mul_f32_e32 v94, 0xbfb8aa3b, v93
	v_exp_f32_e32 v94, v94
	v_fma_f32 v91, v174, v91, v175
	v_fmac_f32_e32 v91, v167, v89
	v_fmac_f32_e32 v91, v168, v87
	v_add_f32_e32 v94, 1.0, v94
; __device__ __forceinline__ float sigmoidf_(float x) { return __builtin_amdgcn_rcpf(1.0f + __expf(-x)); }
; __device__ __forceinline__ bf16_t f2bf(float v) { return (bf16_t)(cvt_pk_bf16(v, 0.f) & 0xffffu); }
; __device__ __forceinline__ void ml_out_phase(const Params& p, Frame& F) {
;     ...
;         { const float q0 = cwv[0], q1 = cwv[1], q2 = cwv[2], q3 = cwv[3], qb = cwv[4], k0 = cwv[5], k1 = cwv[6], k2 = cwv[7], k3 = cwv[8], kb = cwv[9];
; #pragma unroll
;           for (int j = 0; j < 16; ++j) { const float a = qb + q0 * rq[j] + q1 * rq[j + 1] + q2 * rq[j + 2] + q3 * rq[j + 3]; const float bq = kb + k0 * rk[j] + k1 * rk[j + 1] + k2 * rk[j + 2] + k3 * rk[j + 3];
;               const int t = 16 * tq + j, sw = t * 128 + ((((d >> 3) ^ (t & 15)) << 3) | (d & 7));
;               QR[sw] = f2bf(a * sigmoidf_(a) * 0.08838834764831845f); KR[sw] = f2bf(bq * sigmoidf_(bq)); } }
	v_rcp_f32_e32 v94, v94
	v_fmac_f32_e32 v91, v171, v85
	v_fma_f32 v90, v173, v90, v172
	v_fmac_f32_e32 v90, v169, v88
	v_mul_f32_e32 v93, v93, v94
	v_mul_f32_e32 v93, 0x3db504f3, v93
	v_cvt_pk_bf16_f32 v93, v93, s0
	ds_write_b16 v182, v93 offset:1280
	v_mul_f32_e32 v93, 0xbfb8aa3b, v92
	v_exp_f32_e32 v93, v93
	v_fmac_f32_e32 v90, v166, v86
	v_fmac_f32_e32 v90, v170, v84
	v_fma_f32 v89, v174, v89, v175
	v_add_f32_e32 v93, 1.0, v93
	v_rcp_f32_e32 v93, v93
	v_fmac_f32_e32 v89, v167, v87
	v_fmac_f32_e32 v89, v168, v85
	v_fmac_f32_e32 v89, v171, v83
	v_mul_f32_e32 v92, v92, v93
	v_cvt_pk_bf16_f32 v92, v92, s0
	ds_write_b16 v182, v92 offset:18688
	v_mul_f32_e32 v92, 0xbfb8aa3b, v91
	v_exp_f32_e32 v92, v92
	v_fma_f32 v88, v173, v88, v172
	v_fmac_f32_e32 v88, v169, v86
	v_fmac_f32_e32 v88, v166, v84
	v_add_f32_e32 v92, 1.0, v92
	v_rcp_f32_e32 v92, v92
	v_fmac_f32_e32 v88, v170, v82
	v_fma_f32 v87, v174, v87, v175
	v_fmac_f32_e32 v87, v167, v85
	v_mul_f32_e32 v91, v91, v92
	v_mul_f32_e32 v91, 0x3db504f3, v91
	v_cvt_pk_bf16_f32 v91, v91, s0
	ds_write_b16 v183, v91 offset:1536
	v_mul_f32_e32 v91, 0xbfb8aa3b, v90
	v_exp_f32_e32 v91, v91
	v_fmac_f32_e32 v87, v168, v83
	v_fmac_f32_e32 v87, v171, v81
	v_fma_f32 v86, v173, v86, v172
	v_add_f32_e32 v91, 1.0, v91
	v_rcp_f32_e32 v91, v91
	v_fmac_f32_e32 v86, v169, v84
	v_fmac_f32_e32 v86, v166, v82
	v_fmac_f32_e32 v86, v170, v80
	v_mul_f32_e32 v90, v90, v91
	v_cvt_pk_bf16_f32 v90, v90, s0
	ds_write_b16 v183, v90 offset:18944
	v_mul_f32_e32 v90, 0xbfb8aa3b, v89
	v_exp_f32_e32 v90, v90
	v_fma_f32 v85, v174, v85, v175
	v_fmac_f32_e32 v85, v167, v83
	v_fmac_f32_e32 v85, v168, v81
	v_add_f32_e32 v90, 1.0, v90
	v_rcp_f32_e32 v90, v90
	v_fmac_f32_e32 v85, v171, v79
	v_fma_f32 v84, v173, v84, v172
	v_fmac_f32_e32 v84, v169, v82
	v_mul_f32_e32 v89, v89, v90
	v_mul_f32_e32 v89, 0x3db504f3, v89
	v_cvt_pk_bf16_f32 v89, v89, s0
	ds_write_b16 v184, v89 offset:1792
	v_mul_f32_e32 v89, 0xbfb8aa3b, v88
	v_exp_f32_e32 v89, v89
	v_fmac_f32_e32 v84, v166, v80
	v_fmac_f32_e32 v84, v170, v78
	v_fma_f32 v83, v174, v83, v175
	v_add_f32_e32 v89, 1.0, v89
	v_rcp_f32_e32 v89, v89
	v_fmac_f32_e32 v83, v167, v81
	v_fmac_f32_e32 v83, v168, v79
	v_fmac_f32_e32 v83, v171, v77
	v_mul_f32_e32 v88, v88, v89
	v_cvt_pk_bf16_f32 v88, v88, s0
	ds_write_b16 v184, v88 offset:19200
	v_mul_f32_e32 v88, 0xbfb8aa3b, v87
	v_exp_f32_e32 v88, v88
	v_fma_f32 v82, v173, v82, v172
	v_fmac_f32_e32 v82, v169, v80
	v_fmac_f32_e32 v82, v166, v78
	v_add_f32_e32 v88, 1.0, v88
	v_rcp_f32_e32 v88, v88
	v_fmac_f32_e32 v82, v170, v76
	v_fma_f32 v81, v174, v81, v175
	v_fmac_f32_e32 v81, v167, v79
	v_mul_f32_e32 v87, v87, v88
	v_mul_f32_e32 v87, 0x3db504f3, v87
	v_cvt_pk_bf16_f32 v87, v87, s0
	ds_write_b16 v185, v87 offset:2048
	v_mul_f32_e32 v87, 0xbfb8aa3b, v86
	v_exp_f32_e32 v87, v87
	v_fmac_f32_e32 v81, v168, v77
	v_fmac_f32_e32 v81, v171, v75
	v_fma_f32 v80, v173, v80, v172
	v_add_f32_e32 v87, 1.0, v87
	v_rcp_f32_e32 v87, v87
	v_fmac_f32_e32 v80, v169, v78
	v_fmac_f32_e32 v80, v166, v76
	v_fmac_f32_e32 v80, v170, v74
	v_mul_f32_e32 v86, v86, v87
	v_cvt_pk_bf16_f32 v86, v86, s0
	ds_write_b16 v185, v86 offset:19456
	v_mul_f32_e32 v86, 0xbfb8aa3b, v85
	v_exp_f32_e32 v86, v86
	v_fma_f32 v79, v174, v79, v175
	v_fmac_f32_e32 v79, v167, v77
	v_fmac_f32_e32 v79, v168, v75
	v_add_f32_e32 v86, 1.0, v86
	v_rcp_f32_e32 v86, v86
	v_fmac_f32_e32 v79, v171, v70
	v_fma_f32 v78, v173, v78, v172
	v_fmac_f32_e32 v78, v169, v76
	v_mul_f32_e32 v85, v85, v86
	v_mul_f32_e32 v85, 0x3db504f3, v85
	v_cvt_pk_bf16_f32 v85, v85, s0
	ds_write_b16 v186, v85 offset:2304
	v_mul_f32_e32 v85, 0xbfb8aa3b, v84
	v_exp_f32_e32 v85, v85
	v_fmac_f32_e32 v78, v166, v74
	v_fmac_f32_e32 v78, v170, v66
	v_fma_f32 v77, v174, v77, v175
	v_add_f32_e32 v85, 1.0, v85
	v_rcp_f32_e32 v85, v85
	v_fmac_f32_e32 v77, v167, v75
	v_fmac_f32_e32 v77, v168, v70
	v_fmac_f32_e32 v77, v171, v71
	v_mul_f32_e32 v84, v84, v85
	v_cvt_pk_bf16_f32 v84, v84, s0
	ds_write_b16 v186, v84 offset:19712
	v_mul_f32_e32 v84, 0xbfb8aa3b, v83
	v_exp_f32_e32 v84, v84
	v_fma_f32 v76, v173, v76, v172
	v_fmac_f32_e32 v76, v169, v74
	v_fmac_f32_e32 v76, v166, v66
	v_add_f32_e32 v84, 1.0, v84
	v_rcp_f32_e32 v84, v84
	v_fmac_f32_e32 v76, v170, v67
	v_fma_f32 v75, v174, v75, v175
	v_fmac_f32_e32 v75, v167, v70
	v_mul_f32_e32 v83, v83, v84
	v_mul_f32_e32 v83, 0x3db504f3, v83
	v_cvt_pk_bf16_f32 v83, v83, s0
	ds_write_b16 v187, v83 offset:2560
	v_mul_f32_e32 v83, 0xbfb8aa3b, v82
	v_exp_f32_e32 v83, v83
	v_fmac_f32_e32 v75, v168, v71
	v_fmac_f32_e32 v75, v171, v72
	v_fma_f32 v70, v174, v70, v175
	v_add_f32_e32 v83, 1.0, v83
	v_rcp_f32_e32 v83, v83
	v_fma_f32 v74, v173, v74, v172
	v_fmac_f32_e32 v70, v167, v71
	v_fmac_f32_e32 v74, v169, v66
	v_mul_f32_e32 v82, v82, v83
	v_cvt_pk_bf16_f32 v82, v82, s0
	ds_write_b16 v187, v82 offset:19968
	v_mul_f32_e32 v82, 0xbfb8aa3b, v81
	v_exp_f32_e32 v82, v82
	v_fmac_f32_e32 v70, v168, v72
	v_fmac_f32_e32 v74, v166, v67
	v_fmac_f32_e32 v70, v171, v73
	v_add_f32_e32 v82, 1.0, v82
	v_rcp_f32_e32 v82, v82
	v_fma_f32 v66, v173, v66, v172
	v_fmac_f32_e32 v74, v170, v68
	v_fmac_f32_e32 v66, v169, v67
	v_mul_f32_e32 v81, v81, v82
	v_mul_f32_e32 v81, 0x3db504f3, v81
	v_cvt_pk_bf16_f32 v81, v81, s0
	ds_write_b16 v188, v81 offset:2816
	v_mul_f32_e32 v81, 0xbfb8aa3b, v80
	v_exp_f32_e32 v81, v81
; #define LAS __attribute__((address_space(3)))
; __device__ __forceinline__ float sigmoidf_(float x) { return __builtin_amdgcn_rcpf(1.0f + __expf(-x)); }
; #define LBAR() do { asm volatile("s_waitcnt lgkmcnt(0)" ::: "memory"); __builtin_amdgcn_s_barrier(); asm volatile("" ::: "memory"); } while (0)
; __device__ __forceinline__ bf16_t f2bf(float v) { return (bf16_t)(cvt_pk_bf16(v, 0.f) & 0xffffu); }
; __device__ __forceinline__ void ml_out_phase(const Params& p, Frame& F) {
;     ...
;               QR[sw] = f2bf(a * sigmoidf_(a) * 0.08838834764831845f); KR[sw] = f2bf(bq * sigmoidf_(bq)); } }
;         LBAR();
;         { const float* nst = (const float*)(ws + WS_NST) + (size_t)item * 128;
; #pragma unroll
;           for (int ks = 0; ks < 4; ++ks) { nsv[2 * ks] = *(const f32x4*)(nst + 32 * ks + 8 * fq); nsv[2 * ks + 1] = *(const f32x4*)(nst + 32 * ks + 8 * fq + 4); } }
;         __builtin_amdgcn_sched_barrier(0);
;         bf16x8 aq[4];
; #pragma unroll
;         for (int ks = 0; ks < 4; ++ks) aq[ks] = *(const LAS bf16x8*)(QR + (16 * tb + fr) * 128 + (((4 * ks + fq) ^ fr) << 3));
;         float Mr[4], wi[4], rsum[4];
; #pragma unroll
;         for (int i = 0; i < 4; ++i) { const int tl = 16 * tb + 4 * fq + i; Mr[i] = Mvec[tl]; wi[i] = wint[tl]; rsum[i] = 0.f; }
; #pragma unroll
;         for (int sb = 0; sb < 4; ++sb) {
;             f32x4 acc = (f32x4){0.f, 0.f, 0.f, 0.f};
;             if (sb <= tb) {
; #pragma unroll
;                 for (int ks = 0; ks < 4; ++ks) acc = __builtin_amdgcn_mfma_f32_16x16x32_bf16(aq[ks], *(const LAS bf16x8*)(KR + (16 * sb + fr) * 128 + (((4 * ks + fq) ^ fr) << 3)), acc, 0, 0, 0);
;             }
;             const int s = 16 * sb + fr; const float as = avec[s];
; #pragma unroll
;             for (int i = 0; i < 4; ++i) { const int tl = 16 * tb + 4 * fq + i; const float v = (s <= tl) ? acc[i] * __expf(as - Mr[i]) : 0.f; rsum[i] += v; ATT[(4 * fq + i) * TT + s] = f2bf(v); }
	v_mul_f32_e32 v67, 0xbfb8aa3b, v70
	v_exp_f32_e32 v67, v67
	v_fmac_f32_e32 v66, v166, v68
	v_add_f32_e32 v81, 1.0, v81
	v_rcp_f32_e32 v81, v81
	v_add_f32_e32 v67, 1.0, v67
	v_rcp_f32_e32 v67, v67
	v_fmac_f32_e32 v66, v170, v69
	v_mul_f32_e32 v80, v80, v81
	v_cvt_pk_bf16_f32 v80, v80, s0
	ds_write_b16 v188, v80 offset:20224
	v_mul_f32_e32 v80, 0xbfb8aa3b, v79
	v_exp_f32_e32 v80, v80
	v_mul_f32_e32 v67, v70, v67
	v_mul_f32_e32 v67, 0x3db504f3, v67
	v_cvt_pk_bf16_f32 v67, v67, s0
	v_add_f32_e32 v80, 1.0, v80
	v_rcp_f32_e32 v80, v80
	s_nop 0
	v_mul_f32_e32 v79, v79, v80
	v_mul_f32_e32 v79, 0x3db504f3, v79
	v_cvt_pk_bf16_f32 v79, v79, s0
	ds_write_b16 v189, v79 offset:3072
	v_mul_f32_e32 v79, 0xbfb8aa3b, v78
	v_exp_f32_e32 v79, v79
	s_nop 0
	v_add_f32_e32 v79, 1.0, v79
	v_rcp_f32_e32 v79, v79
	s_nop 0
	v_mul_f32_e32 v78, v78, v79
	v_cvt_pk_bf16_f32 v78, v78, s0
	ds_write_b16 v189, v78 offset:20480
	v_mul_f32_e32 v78, 0xbfb8aa3b, v77
	v_exp_f32_e32 v78, v78
	s_nop 0
	v_add_f32_e32 v78, 1.0, v78
	v_rcp_f32_e32 v78, v78
	s_nop 0
	v_mul_f32_e32 v77, v77, v78
	v_mul_f32_e32 v77, 0x3db504f3, v77
	v_cvt_pk_bf16_f32 v77, v77, s0
	ds_write_b16 v190, v77 offset:3328
	v_mul_f32_e32 v77, 0xbfb8aa3b, v76
	v_exp_f32_e32 v77, v77
	s_nop 0
	v_add_f32_e32 v77, 1.0, v77
	v_rcp_f32_e32 v77, v77
	s_nop 0
	v_mul_f32_e32 v76, v76, v77
	v_cvt_pk_bf16_f32 v76, v76, s0
	ds_write_b16 v190, v76 offset:20736
	v_mul_f32_e32 v76, 0xbfb8aa3b, v75
	v_exp_f32_e32 v76, v76
	s_nop 0
	v_add_f32_e32 v76, 1.0, v76
	v_rcp_f32_e32 v76, v76
	s_nop 0
	v_mul_f32_e32 v75, v75, v76
	v_mul_f32_e32 v75, 0x3db504f3, v75
	v_cvt_pk_bf16_f32 v75, v75, s0
	ds_write_b16 v191, v75 offset:3584
	v_mul_f32_e32 v75, 0xbfb8aa3b, v74
	v_exp_f32_e32 v75, v75
	s_nop 0
	v_add_f32_e32 v75, 1.0, v75
	v_rcp_f32_e32 v75, v75
	s_nop 0
	v_mul_f32_e32 v74, v74, v75
	v_cvt_pk_bf16_f32 v74, v74, s0
	ds_write_b16 v191, v74 offset:20992
	ds_write_b16 v192, v67 offset:3840
	v_mul_f32_e32 v67, 0xbfb8aa3b, v66
	v_exp_f32_e32 v67, v67
	s_nop 0
	v_add_f32_e32 v67, 1.0, v67
	v_rcp_f32_e32 v67, v67
	s_nop 0
	v_mul_f32_e32 v66, v66, v67
	v_cvt_pk_bf16_f32 v66, v66, s0
	ds_write_b16 v192, v66 offset:21248
	s_lshl_b64 s[0:1], s[90:91], 9
	s_waitcnt vmcnt(21)
	s_waitcnt lgkmcnt(0)
	s_barrier
	v_lshl_add_u64 v[66:67], v[130:131], 0, s[0:1]
	global_load_dwordx4 v[110:113], v[66:67], off offset:16
	global_load_dwordx4 v[114:117], v[66:67], off
	global_load_dwordx4 v[102:105], v[66:67], off offset:144
	global_load_dwordx4 v[106:109], v[66:67], off offset:128
	global_load_dwordx4 v[94:97], v[66:67], off offset:272
	global_load_dwordx4 v[98:101], v[66:67], off offset:256
	global_load_dwordx4 v[86:89], v[66:67], off offset:400
	global_load_dwordx4 v[90:93], v[66:67], off offset:384
	v_add_u32_e32 v66, v161, v1
	ds_read_b128 v[82:85], v66
	v_add_u32_e32 v66, v161, v193
	ds_read_b128 v[78:81], v66
	v_add_u32_e32 v66, v161, v194
	ds_read_b128 v[74:77], v66
	v_add_u32_e32 v66, v161, v195
	v_add_u32_e32 v225, v163, v1
	ds_read_b128 v[70:73], v66
	ds_read_b128 v[118:121], v196
	ds_read_b128 v[66:69], v197
	ds_read_b128 v[122:125], v225 offset:17408
	ds_read_b32 v126, v198
	v_add_u32_e32 v228, v163, v193
	ds_read_b128 v[230:233], v228 offset:17408
	s_waitcnt lgkmcnt(0)
	v_mfma_f32_16x16x32_bf16 v[122:125], v[82:85], v[122:125], 0
	v_add_u32_e32 v227, v163, v194
	v_add_u32_e32 v226, v163, v195
	v_sub_f32_e32 v127, v126, v118
	v_mfma_f32_16x16x32_bf16 v[122:125], v[78:81], v[230:233], v[122:125]
	ds_read_b128 v[230:233], v227 offset:17408
	v_mul_f32_e32 v127, 0x3fb8aa3b, v127
	v_exp_f32_e32 v127, v127
	s_waitcnt lgkmcnt(0)
	v_mfma_f32_16x16x32_bf16 v[122:125], v[74:77], v[230:233], v[122:125]
	ds_read_b128 v[230:233], v226 offset:17408
	s_andn2_b64 vcc, exec, s[52:53]
	s_waitcnt lgkmcnt(0)
	v_mfma_f32_16x16x32_bf16 v[122:125], v[70:73], v[230:233], v[122:125]
	s_nop 7
	v_mul_f32_e32 v122, v122, v127
	v_cndmask_b32_e64 v229, v122, 0, s[30:31]
	v_cvt_pk_bf16_f32 v122, v229, s0
	ds_write_b16 v224, v122
	v_sub_f32_e32 v122, v126, v119
	v_mul_f32_e32 v122, 0x3fb8aa3b, v122
	v_exp_f32_e32 v122, v122
	s_nop 0
	v_mul_f32_e32 v122, v123, v122
	v_cndmask_b32_e64 v230, v122, 0, s[86:87]
	v_cvt_pk_bf16_f32 v122, v230, s0
	ds_write_b16 v224, v122 offset:144
	v_sub_f32_e32 v122, v126, v120
	v_mul_f32_e32 v122, 0x3fb8aa3b, v122
	v_exp_f32_e32 v122, v122
	s_nop 0
	v_mul_f32_e32 v122, v124, v122
	v_cndmask_b32_e64 v231, v122, 0, s[64:65]
	v_cvt_pk_bf16_f32 v122, v231, s0
	ds_write_b16 v224, v122 offset:288
	v_sub_f32_e32 v122, v126, v121
	v_mul_f32_e32 v122, 0x3fb8aa3b, v122
	v_exp_f32_e32 v122, v122
	s_nop 0
	v_mul_f32_e32 v122, v125, v122
	v_cndmask_b32_e64 v232, v122, 0, s[56:57]
	v_cvt_pk_bf16_f32 v122, v232, s0
	ds_write_b16 v224, v122 offset:432
	s_cbranch_vccnz .LBB0_618
	ds_read_b128 v[122:125], v225 offset:21504
	ds_read_b128 v[234:237], v228 offset:21504
	s_waitcnt lgkmcnt(0)
	v_mfma_f32_16x16x32_bf16 v[122:125], v[82:85], v[122:125], 0
	v_mfma_f32_16x16x32_bf16 v[122:125], v[78:81], v[234:237], v[122:125]
	ds_read_b128 v[234:237], v227 offset:21504
	s_waitcnt lgkmcnt(0)
	v_mfma_f32_16x16x32_bf16 v[122:125], v[74:77], v[234:237], v[122:125]
	ds_read_b128 v[234:237], v226 offset:21504
	s_waitcnt lgkmcnt(0)
	v_mfma_f32_16x16x32_bf16 v[122:125], v[70:73], v[234:237], v[122:125]
	s_branch .LBB0_619

; __device__ __forceinline__ void ml_out_phase(const Params& p, Frame& F) {
;     ...
;         { const bf16_t* CT = (const bf16_t*)(ws + WS_CST) + (size_t)item * 32768;
; #pragma unroll
;           for (int nb = 0; nb < 4; ++nb)
; #pragma unroll
;               for (int ks = 0; ks < 4; ++ks) ctg[nb][ks] = *(const bf16x8*)(CT + (size_t)(16 * (8 * vh + 4 + nb) + fr) * 128 + 32 * ks + 8 * fq); }
;         __builtin_amdgcn_sched_barrier(0);
;         asm volatile("s_waitcnt lgkmcnt(0)" ::: "memory");
;         bf16x8 aa[2];
; #pragma unroll
;         for (int ks = 0; ks < 2; ++ks) aa[ks] = lds_frag(ATT, fr, TT, 32 * ks + 8 * fq);
; #pragma unroll
;         for (int nb = 0; nb < 4; ++nb) { const int vrow = 16 * (8 * vh + nb) + fr;
; #pragma unroll
;             for (int ks = 0; ks < 2; ++ks) o[nb] = __builtin_amdgcn_mfma_f32_16x16x32_bf16(aa[ks], lds_frag(VT, vrow, TT, 32 * ks + 8 * fq), o[nb], 0, 0, 0); }
;         __builtin_amdgcn_sched_barrier(0);
; #pragma unroll
;         for (int nb = 4; nb < 8; ++nb) { o[nb] = (f32x4){0.f, 0.f, 0.f, 0.f};
; #pragma unroll
;             for (int ks = 0; ks < 4; ++ks) o[nb] = __builtin_amdgcn_mfma_f32_16x16x32_bf16(aq[ks], ctg[nb - 4][ks], o[nb], 0, 0, 0);
; #pragma unroll
;             for (int i = 0; i < 4; ++i) o[nb][i] *= wi[i];
;             const int vrow = 16 * (8 * vh + nb) + fr;
; #pragma unroll
;             for (int ks = 0; ks < 2; ++ks) o[nb] = __builtin_amdgcn_mfma_f32_16x16x32_bf16(aa[ks], lds_frag(VT, vrow, TT, 32 * ks + 8 * fq), o[nb], 0, 0, 0); }
.LBB0_625:
	s_or_b64 exec, exec, s[0:1]
	s_waitcnt lgkmcnt(4)
	v_add_f32_e32 v63, v38, v30
	s_waitcnt lgkmcnt(3)
	v_add_f32_e32 v64, v22, v23
	s_waitcnt lgkmcnt(2)
	v_add_f32_e32 v65, v24, v10
	s_waitcnt lgkmcnt(1)
	v_add_f32_e32 v61, v11, v12
	s_waitcnt lgkmcnt(0)
	ds_read_b128 v[22:25], v246
	ds_read_b128 v[26:29], v246 offset:1024
	ds_read_b128 v[86:89], v246 offset:2048
	ds_read_b128 v[90:93], v246 offset:3072
	ds_read_b128 v[94:97], v246 offset:4096
	ds_read_b128 v[98:101], v246 offset:5120
	ds_read_b128 v[102:105], v246 offset:6144
	ds_read_b128 v[106:109], v246 offset:7168
	ds_read_b128 v[110:113], v246 offset:8192
	ds_read_b128 v[114:117], v246 offset:9216
	ds_read_b128 v[118:121], v246 offset:10240
	ds_read_b128 v[122:125], v246 offset:11264
	ds_read_b128 v[226:229], v246 offset:12288
	ds_read_b128 v[46:49], v246 offset:13312
	ds_read_b128 v[42:45], v246 offset:14336
	ds_read_b128 v[38:41], v246 offset:15360
	ds_read_b128 v[34:37], v219
	ds_read_b128 v[30:33], v219 offset:64
	ds_read_b128 v[2:5], v220
	v_pk_mul_f32 v[8:9], v[68:69], v[56:57]
	s_waitcnt lgkmcnt(3)
	v_pk_mul_f32 v[6:7], v[66:67], v[54:55]
	v_pk_mul_f32 v[12:13], v[68:69], v[52:53]
	v_pk_mul_f32 v[10:11], v[66:67], v[50:51]
	s_waitcnt lgkmcnt(0)
	v_mfma_f32_16x16x32_bf16 v[2:5], v[34:37], v[2:5], v[6:9]
	v_mul_f32_e64 v20, v68, v20
	v_mul_f32_e64 v21, v69, v21
	v_pk_mul_f32 v[18:19], v[66:67], v[18:19]
	v_pk_mul_f32 v[16:17], v[68:69], v[16:17]
	ds_read_b128 v[6:9], v220 offset:64
	s_waitcnt lgkmcnt(0)
	v_mfma_f32_16x16x32_bf16 v[2:5], v[30:33], v[6:9], v[2:5]
	ds_read_b128 v[6:9], v220 offset:2304
	v_pk_mul_f32 v[14:15], v[66:67], v[14:15]
	s_waitcnt lgkmcnt(0)
	v_mfma_f32_16x16x32_bf16 v[6:9], v[34:37], v[6:9], v[10:13]
	s_nop 2
	ds_read_b128 v[10:13], v220 offset:2368
	s_waitcnt lgkmcnt(0)
	v_mfma_f32_16x16x32_bf16 v[6:9], v[30:33], v[10:13], v[6:9]
	ds_read_b128 v[10:13], v220 offset:4608
	s_waitcnt lgkmcnt(0)
	v_mfma_f32_16x16x32_bf16 v[10:13], v[34:37], v[10:13], v[18:21]
	s_nop 2
	ds_read_b128 v[18:21], v220 offset:4672
	s_waitcnt lgkmcnt(0)
	v_mfma_f32_16x16x32_bf16 v[10:13], v[30:33], v[18:21], v[10:13]
	ds_read_b128 v[18:21], v220 offset:6912
	s_waitcnt lgkmcnt(0)
	v_mfma_f32_16x16x32_bf16 v[14:17], v[34:37], v[18:21], v[14:17]
	ds_read_b128 v[18:21], v220 offset:6976
	s_waitcnt lgkmcnt(0)
	v_mfma_f32_16x16x32_bf16 v[14:17], v[30:33], v[18:21], v[14:17]
	s_waitcnt lgkmcnt(0)
	v_mfma_f32_16x16x32_bf16 v[18:21], v[82:85], v[22:25], 0
	ds_read_b128 v[22:25], v220 offset:9216
	ds_read_b128 v[50:53], v220 offset:13824
	v_mfma_f32_16x16x32_bf16 v[18:21], v[78:81], v[26:29], v[18:21]
	ds_read_b128 v[26:29], v220 offset:11520
	v_mfma_f32_16x16x32_bf16 v[18:21], v[74:77], v[86:89], v[18:21]
	v_mfma_f32_16x16x32_bf16 v[18:21], v[70:73], v[90:93], v[18:21]
	s_nop 7
	v_pk_mul_f32 v[20:21], v[68:69], v[20:21]
	v_pk_mul_f32 v[18:19], v[66:67], v[18:19]
	s_waitcnt lgkmcnt(2)
	s_nop 0
	v_mfma_f32_16x16x32_bf16 v[18:21], v[34:37], v[22:25], v[18:21]
	ds_read_b128 v[22:25], v220 offset:9280
	s_waitcnt lgkmcnt(0)
	v_mfma_f32_16x16x32_bf16 v[18:21], v[30:33], v[22:25], v[18:21]
	v_mfma_f32_16x16x32_bf16 v[22:25], v[82:85], v[94:97], 0
	v_mfma_f32_16x16x32_bf16 v[22:25], v[78:81], v[98:101], v[22:25]
	v_mfma_f32_16x16x32_bf16 v[22:25], v[74:77], v[102:105], v[22:25]
	v_mfma_f32_16x16x32_bf16 v[22:25], v[70:73], v[106:109], v[22:25]
	s_nop 7
	v_pk_mul_f32 v[24:25], v[68:69], v[24:25]
	v_pk_mul_f32 v[22:23], v[66:67], v[22:23]
	s_nop 1
	v_mfma_f32_16x16x32_bf16 v[22:25], v[34:37], v[26:29], v[22:25]
	ds_read_b128 v[26:29], v220 offset:11584
	s_waitcnt lgkmcnt(0)
	v_mfma_f32_16x16x32_bf16 v[22:25], v[30:33], v[26:29], v[22:25]
	v_mfma_f32_16x16x32_bf16 v[26:29], v[82:85], v[110:113], 0
	v_mfma_f32_16x16x32_bf16 v[26:29], v[78:81], v[114:117], v[26:29]
	v_mfma_f32_16x16x32_bf16 v[26:29], v[74:77], v[118:121], v[26:29]
	v_mfma_f32_16x16x32_bf16 v[26:29], v[70:73], v[122:125], v[26:29]
	s_nop 7
	v_pk_mul_f32 v[28:29], v[68:69], v[28:29]
	v_pk_mul_f32 v[26:27], v[66:67], v[26:27]
	s_nop 1
	v_mfma_f32_16x16x32_bf16 v[26:29], v[34:37], v[50:53], v[26:29]
	ds_read_b128 v[50:53], v220 offset:13888
	s_waitcnt lgkmcnt(0)
	v_mfma_f32_16x16x32_bf16 v[26:29], v[30:33], v[50:53], v[26:29]
	v_mfma_f32_16x16x32_bf16 v[50:53], v[82:85], v[226:229], 0
	v_mfma_f32_16x16x32_bf16 v[46:49], v[78:81], v[46:49], v[50:53]
	v_mfma_f32_16x16x32_bf16 v[42:45], v[74:77], v[42:45], v[46:49]
	s_nop 3
	ds_read_b128 v[52:55], v165
	s_nop 0
	ds_read_b128 v[48:51], v164
	v_mfma_f32_16x16x32_bf16 v[38:41], v[70:73], v[38:41], v[42:45]
	s_waitcnt lgkmcnt(0)
; __device__ __forceinline__ void ml_out_phase(const Params& p, Frame& F) {
;     ...
;             for (int ks = 0; ks < 2; ++ks) o[nb] = __builtin_amdgcn_mfma_f32_16x16x32_bf16(aa[ks], lds_frag(VT, vrow, TT, 32 * ks + 8 * fq), o[nb], 0, 0, 0); }
;         __builtin_amdgcn_sched_barrier(0);
; #pragma unroll
;         for (int nb = 4; nb < 8; ++nb) { o[nb] = (f32x4){0.f, 0.f, 0.f, 0.f};
; #pragma unroll
;             for (int ks = 0; ks < 4; ++ks) o[nb] = __builtin_amdgcn_mfma_f32_16x16x32_bf16(aq[ks], ctg[nb - 4][ks], o[nb], 0, 0, 0);
; #pragma unroll
;             for (int i = 0; i < 4; ++i) o[nb][i] *= wi[i];
;             const int vrow = 16 * (8 * vh + nb) + fr;
; #pragma unroll
;             for (int ks = 0; ks < 2; ++ks) o[nb] = __builtin_amdgcn_mfma_f32_16x16x32_bf16(aa[ks], lds_frag(VT, vrow, TT, 32 * ks + 8 * fq), o[nb], 0, 0, 0); }
;         float sq[4];
; #pragma unroll
;         for (int i = 0; i < 4; ++i) { const int tl = 16 * tb + 4 * fq + i; const float den = wi[i] * qnl[w * 16 + 4 * fq + i] + rsum[i]; const float inv = 1.0f / fmaxf(fabsf(den), eneg[tl]);
;             float s = 0.f;
; #pragma unroll
;             for (int nb = 0; nb < 8; ++nb) { o[nb][i] *= inv; s += o[nb][i] * o[nb][i]; }
;             s += __shfl_xor(s, 1); s += __shfl_xor(s, 2); s += __shfl_xor(s, 4); s += __shfl_xor(s, 8); sq[i] = s; }
;         if (fr == 0) {
; #pragma unroll
;             for (int i = 0; i < 4; ++i) ssqp[vh * 64 + 16 * tb + 4 * fq + i] = sq[i]; }
	v_fmac_f32_e32 v64, v67, v49
	s_nop 0
	ds_read_b128 v[42:45], v220 offset:16128
	s_nop 3
	v_pk_mul_f32 v[40:41], v[68:69], v[40:41]
	v_pk_mul_f32 v[38:39], v[66:67], v[38:39]
	v_fmac_f32_e32 v63, v66, v48
	v_fmac_f32_e32 v61, v69, v51
	s_waitcnt lgkmcnt(0)
	v_mfma_f32_16x16x32_bf16 v[34:37], v[34:37], v[42:45], v[38:41]
	v_fmac_f32_e32 v65, v68, v50
	s_nop 1
	ds_read_b128 v[38:41], v220 offset:16192
	s_waitcnt lgkmcnt(0)
	v_mfma_f32_16x16x32_bf16 v[30:33], v[30:33], v[38:41], v[34:37]
	s_nop 2
	v_max_f32_e32 v35, v53, v53
	v_max_f32_e64 v35, |v64|, v35
	v_div_scale_f32 v36, s[0:1], v35, v35, 1.0
	v_rcp_f32_e32 v37, v36
	v_max_f32_e32 v34, v52, v52
	v_max_f32_e64 v34, |v63|, v34
	v_fma_f32 v38, -v36, v37, 1.0
	v_fmac_f32_e32 v37, v38, v37
	v_div_scale_f32 v38, vcc, 1.0, v35, 1.0
	v_mul_f32_e32 v39, v38, v37
	v_fma_f32 v40, -v36, v39, v38
	v_fmac_f32_e32 v39, v40, v37
	v_fma_f32 v36, -v36, v39, v38
	v_div_fmas_f32 v36, v36, v37, v39
	v_div_fixup_f32 v35, v36, v35, 1.0
	v_div_scale_f32 v36, s[0:1], v34, v34, 1.0
	v_rcp_f32_e32 v37, v36
	s_nop 0
	v_fma_f32 v38, -v36, v37, 1.0
	v_fmac_f32_e32 v37, v38, v37
	v_div_scale_f32 v38, vcc, 1.0, v34, 1.0
	v_mul_f32_e32 v39, v38, v37
	v_fma_f32 v40, -v36, v39, v38
	v_fmac_f32_e32 v39, v40, v37
	v_fma_f32 v36, -v36, v39, v38
	v_div_fmas_f32 v36, v36, v37, v39
	v_div_fixup_f32 v34, v36, v34, 1.0
	v_pk_mul_f32 v[44:45], v[10:11], v[34:35]
	v_max_f32_e32 v11, v55, v55
	v_max_f32_e64 v11, |v61|, v11
	v_pk_mul_f32 v[42:43], v[14:15], v[34:35]
	v_div_scale_f32 v14, s[0:1], v11, v11, 1.0
	v_rcp_f32_e32 v15, v14
	v_pk_mul_f32 v[40:41], v[18:19], v[34:35]
	v_pk_mul_f32 v[38:39], v[22:23], v[34:35]
	v_max_f32_e32 v10, v54, v54
	v_fma_f32 v18, -v14, v15, 1.0
	v_fmac_f32_e32 v15, v18, v15
	v_div_scale_f32 v18, vcc, 1.0, v11, 1.0
	v_mul_f32_e32 v19, v18, v15
	v_fma_f32 v22, -v14, v19, v18
	v_fmac_f32_e32 v19, v22, v15
	v_fma_f32 v14, -v14, v19, v18
	v_max_f32_e64 v10, |v65|, v10
	v_div_fmas_f32 v14, v14, v15, v19
	v_div_fixup_f32 v11, v14, v11, 1.0
	v_div_scale_f32 v14, s[0:1], v10, v10, 1.0
	v_rcp_f32_e32 v15, v14
	v_pk_mul_f32 v[46:47], v[6:7], v[34:35]
	v_pk_mul_f32 v[36:37], v[26:27], v[34:35]
	v_pk_mul_f32 v[48:49], v[2:3], v[34:35]
	v_fma_f32 v18, -v14, v15, 1.0
	v_fmac_f32_e32 v15, v18, v15
	v_div_scale_f32 v18, vcc, 1.0, v10, 1.0
	v_mul_f32_e32 v19, v18, v15
	v_fma_f32 v22, -v14, v19, v18
	v_fmac_f32_e32 v19, v22, v15
	v_fma_f32 v14, -v14, v19, v18
	v_div_fmas_f32 v14, v14, v15, v19
	v_div_fixup_f32 v10, v14, v10, 1.0
	v_pk_mul_f32 v[26:27], v[8:9], v[10:11]
	v_pk_mul_f32 v[2:3], v[46:47], v[46:47]
	v_pk_mul_f32 v[34:35], v[30:31], v[34:35]
	v_pk_mul_f32 v[30:31], v[4:5], v[10:11]
	v_pk_mul_f32 v[4:5], v[26:27], v[26:27]
	v_pk_fma_f32 v[2:3], v[48:49], v[48:49], v[2:3]
	v_pk_fma_f32 v[4:5], v[30:31], v[30:31], v[4:5]
	v_pk_mul_f32 v[22:23], v[12:13], v[10:11]
	v_pk_fma_f32 v[2:3], v[44:45], v[44:45], v[2:3]
	v_pk_fma_f32 v[4:5], v[22:23], v[22:23], v[4:5]
	v_pk_mul_f32 v[18:19], v[16:17], v[10:11]
	v_pk_fma_f32 v[2:3], v[42:43], v[42:43], v[2:3]
	v_pk_fma_f32 v[4:5], v[18:19], v[18:19], v[4:5]
	v_pk_mul_f32 v[16:17], v[20:21], v[10:11]
	v_pk_fma_f32 v[2:3], v[40:41], v[40:41], v[2:3]
	v_pk_fma_f32 v[4:5], v[16:17], v[16:17], v[4:5]
	v_pk_mul_f32 v[14:15], v[24:25], v[10:11]
	v_pk_fma_f32 v[2:3], v[38:39], v[38:39], v[2:3]
	v_pk_fma_f32 v[4:5], v[14:15], v[14:15], v[4:5]
	v_pk_mul_f32 v[12:13], v[28:29], v[10:11]
	v_pk_fma_f32 v[2:3], v[36:37], v[36:37], v[2:3]
	v_pk_fma_f32 v[4:5], v[12:13], v[12:13], v[4:5]
	v_pk_mul_f32 v[10:11], v[32:33], v[10:11]
	v_pk_fma_f32 v[2:3], v[34:35], v[34:35], v[2:3]
	v_pk_fma_f32 v[4:5], v[10:11], v[10:11], v[4:5]
	ds_bpermute_b32 v6, v62, v2
	ds_bpermute_b32 v7, v62, v3
	ds_bpermute_b32 v8, v62, v4
	ds_bpermute_b32 v9, v62, v5
	s_waitcnt lgkmcnt(2)
	v_pk_add_f32 v[2:3], v[2:3], v[6:7]
	ds_bpermute_b32 v6, v60, v2
	s_waitcnt lgkmcnt(1)
	v_pk_add_f32 v[4:5], v[4:5], v[8:9]
	ds_bpermute_b32 v7, v60, v3
	ds_bpermute_b32 v8, v60, v4
	ds_bpermute_b32 v9, v60, v5
	s_waitcnt lgkmcnt(2)
	v_pk_add_f32 v[2:3], v[2:3], v[6:7]
	ds_bpermute_b32 v6, v59, v2
	s_waitcnt lgkmcnt(1)
	v_pk_add_f32 v[4:5], v[4:5], v[8:9]
	ds_bpermute_b32 v7, v59, v3
	ds_bpermute_b32 v8, v59, v4
	ds_bpermute_b32 v9, v59, v5
	s_waitcnt lgkmcnt(2)
	v_pk_add_f32 v[2:3], v[2:3], v[6:7]
	ds_bpermute_b32 v6, v58, v2
	s_waitcnt lgkmcnt(1)
	v_pk_add_f32 v[4:5], v[4:5], v[8:9]
	ds_bpermute_b32 v7, v58, v3
	ds_bpermute_b32 v8, v58, v4
	ds_bpermute_b32 v9, v58, v5
	s_and_saveexec_b64 s[0:1], s[18:19]
	s_cbranch_execz .LBB0_627
	v_readlane_b32 s4, v244, 2
	s_waitcnt lgkmcnt(2)
	v_pk_add_f32 v[2:3], v[2:3], v[6:7]
	v_add_u32_e32 v6, s4, v162
	ds_write2_b32 v6, v2, v3 offset1:1
	s_waitcnt lgkmcnt(1)
	v_pk_add_f32 v[2:3], v[4:5], v[8:9]
	ds_write2_b32 v6, v2, v3 offset0:2 offset1:3
